# baseline (speedup 1.0000x reference)
.LBB0_35:
	s_or_b64 exec, exec, s[0:1]
	s_waitcnt vmcnt(14)
	v_mul_u32_u24_e32 v105, 0x880, v227
	s_waitcnt vmcnt(11)
	v_cvt_pk_f16_f32 v3, v150, v151
	v_cvt_pk_f16_f32 v2, v148, v149
	v_lshl_add_u32 v4, v1, 1, v105
	s_waitcnt vmcnt(10)
	v_cvt_pk_f16_f32 v1, v154, v155
	s_waitcnt lgkmcnt(0)
	v_cvt_pk_f16_f32 v0, v152, v153
	s_barrier
	v_lshl_or_b32 v233, v225, 6, v220
	v_mul_u32_u24_e32 v233, 0x110, v233
	v_add_u32_e32 v233, v233, v223
	v_add_u32_e32 v233, 0x10000, v233
	ds_read_b128 v[180:183], v233
	ds_read_b128 v[184:187], v233 offset:32
	ds_read_b128 v[188:191], v233 offset:64
	ds_read_b128 v[192:195], v233 offset:96
	ds_read_b128 v[196:199], v233 offset:128
	ds_read_b128 v[200:203], v233 offset:160
	ds_read_b128 v[204:207], v233 offset:192
	ds_read_b128 v[208:211], v233 offset:224
	ds_write2_b64 v4, v[2:3], v[0:1] offset1:34
	s_waitcnt vmcnt(9)
	v_cvt_pk_f16_f32 v1, v166, v167
	v_cvt_pk_f16_f32 v0, v164, v165
	s_waitcnt vmcnt(8)
	v_cvt_pk_f16_f32 v3, v158, v159
	v_cvt_pk_f16_f32 v2, v156, v157
	ds_write2_b64 v4, v[0:1], v[2:3] offset0:68 offset1:102
	s_waitcnt vmcnt(7)
	v_cvt_pk_f16_f32 v1, v162, v163
	v_cvt_pk_f16_f32 v0, v160, v161
	s_waitcnt vmcnt(6)
	v_cvt_pk_f16_f32 v3, v170, v171
	v_cvt_pk_f16_f32 v2, v168, v169
	ds_write2_b64 v4, v[0:1], v[2:3] offset0:136 offset1:170
	s_waitcnt vmcnt(5)
	v_cvt_pk_f16_f32 v1, v174, v175
	v_cvt_pk_f16_f32 v0, v172, v173
	s_waitcnt vmcnt(4)
	v_cvt_pk_f16_f32 v3, v178, v179
	v_cvt_pk_f16_f32 v2, v176, v177
	ds_write2_b64 v4, v[0:1], v[2:3] offset0:204 offset1:238
	ds_read_b128 v[148:151], v233 offset:8704
	ds_read_b128 v[152:155], v233 offset:8736
	ds_read_b128 v[156:159], v233 offset:8768
	ds_read_b128 v[160:163], v233 offset:8800
	ds_read_b128 v[164:167], v233 offset:8832
	ds_read_b128 v[168:171], v233 offset:8864
	ds_read_b128 v[172:175], v233 offset:8896
	ds_read_b128 v[176:179], v233 offset:8928
	v_lshlrev_b32_e32 v2, 1, v228
	s_sleep 16
	s_waitcnt vmcnt(1)
	v_cvt_pk_f16_f32 v1, v40, v41
	v_cvt_pk_f16_f32 v0, v38, v39
	v_mad_u32_u24 v3, v227, s6, v2
	ds_write_b64 v3, v[0:1] offset:34816
	s_waitcnt vmcnt(0)
	v_cvt_pk_f16_f32 v1, v36, v37
	v_cvt_pk_f16_f32 v0, v34, v35
	v_mad_u32_u24 v2, v229, s6, v2
	ds_write_b64 v2, v[0:1] offset:34816
	v_mov_b32_e32 v97, 0
	v_mov_b32_e32 v0, 0
	v_mov_b32_e32 v4, 0
	v_mov_b32_e32 v96, 0
	s_and_saveexec_b64 s[0:1], vcc
	s_cbranch_execz .LBB0_37
	v_lshl_add_u32 v1, v220, 1, v230
	v_or_b32_e32 v2, 0x21000, v1
	v_add_u32_e32 v1, 0x21040, v1
	ds_read_u16 v1, v1
	ds_read_u16 v2, v2
	v_cvt_f16_f32_e32 v0, v104
	s_waitcnt lgkmcnt(1)
	v_and_b32_e32 v4, 0xffff, v1
	v_pack_b32_f16 v0, v0, 0
	s_waitcnt lgkmcnt(0)
	v_and_b32_e32 v96, 0xffff, v2
